# phase 12 (PEER value sums) hand-scheduled: same algorithm and numerics as the baseline (fp8->f32 converts, packed f32 FMAs), permlane-swap lane-group reduction, single table buffer with one-for-one lo
# speedup vs baseline: 1.0247x; 1.0132x over previous
.LBB0_1188:
	s_cmp_lt_i32 s40, 13
	s_cselect_b64 s[2:3], -1, 0
	s_and_b64 s[14:15], s[2:3], s[4:5]
	s_andn2_b64 vcc, exec, s[14:15]
	s_cbranch_vccnz .LBB0_1215
	s_mov_b64 s[2:3], s[0:1]
	s_waitcnt vmcnt(0) lgkmcnt(0)
	v_mbcnt_lo_u32_b32 v0, -1, 0
	v_mbcnt_hi_u32_b32 v0, -1, v0
	s_load_dwordx2 s[4:5], s[2:3], 0xb8
	v_and_b32_e32 v9, 7, v0
	v_lshrrev_b32_e32 v10, 3, v0
	v_lshlrev_b32_e32 v1, 4, v9
	v_lshlrev_b32_e32 v2, 5, v10
	v_lshlrev_b32_e32 v3, 5, v9
	v_and_b32_e32 v11, 56, v0
	v_lshrrev_b32_e32 v11, 1, v11
	v_or_b32_e32 v3, v3, v11
	v_and_b32_e32 v12, 8, v0
	v_cmp_eq_u32_e64 s[44:45], 0, v12
	v_mov_b32_e32 v5, 0
	v_mov_b32_e32 v7, -1
	s_mov_b32 s47, 7
	s_mov_b32 s38, 0x200000
	s_mov_b32 s39, 0x20000
	s_lshl_b32 s16, s24, 1
	s_and_b32 s16, s16, 14
	s_mov_b32 s17, 0
	s_waitcnt lgkmcnt(0)
	s_add_u32 s28, s4, 0x18800000
	s_addc_u32 s29, s5, 0
	s_add_u32 s30, s4, 0x18000000
	s_addc_u32 s31, s5, 0
.Lv_slice:
	s_lshl_b32 s2, s16, 8
	s_add_u32 s6, s4, s2
	s_addc_u32 s7, s5, 0
	s_add_u32 s6, s6, 0x122000
	s_addc_u32 s7, s7, 0
	s_add_u32 s34, s4, s2
	s_addc_u32 s35, s5, 0
	s_add_u32 s34, s34, 0x10000000
	s_addc_u32 s35, s35, 0
	s_lshl_b32 s2, s16, 21
	s_add_u32 s36, s4, s2
	s_addc_u32 s37, s5, 0
	s_add_u32 s36, s36, 0x6000000
	s_addc_u32 s37, s37, 0
	s_and_b32 s37, s37, 0xffff
	s_mov_b64 exec, 1
	global_atomic_inc v6, v5, v7, s[6:7] sc0
	s_waitcnt vmcnt(0)
	v_readfirstlane_b32 s23, v6
	global_atomic_inc v6, v5, v7, s[6:7] sc0
	s_mov_b64 exec, -1
	s_mov_b32 s26, 0
	s_mov_b32 s27, 0
	s_cmp_lg_u32 s26, 32
	s_cbranch_scc1 .Lv_norot_p0
	v_readfirstlane_b32 s23, v6
	s_mov_b64 exec, 1
	global_atomic_inc v6, v5, v7, s[6:7] sc0
	s_mov_b64 exec, -1
	s_mov_b32 s26, 0

.Lv_got_p1:
	s_mov_b32 s21, s22
	s_mov_b32 s49, s50
	s_cmp_eq_u32 s48, 0
	s_cbranch_scc1 .Lv_next_slice
	s_lshl_b32 s2, s20, 8
	s_add_u32 s2, s28, s2
	s_addc_u32 s3, s29, 0
	global_load_dwordx4 v[8:11], v2, s[2:3]
	global_load_dwordx4 v[12:15], v2, s[2:3] offset:16
	s_lshl_b32 s2, s20, 8
	s_add_u32 s2, s30, s2
	s_addc_u32 s3, s31, 0
	global_load_dwordx4 v[24:27], v2, s[2:3]
	global_load_dwordx4 v[28:31], v2, s[2:3] offset:16
	s_lshl_b32 s2, s21, 8
	s_add_u32 s2, s28, s2
	s_addc_u32 s3, s29, 0
	global_load_dwordx4 v[16:19], v2, s[2:3]
	global_load_dwordx4 v[20:23], v2, s[2:3] offset:16
	s_waitcnt vmcnt(0)
	v_lshlrev_b32_sdwa v112, s47, v8 dst_sel:DWORD dst_unused:UNUSED_PAD src0_sel:DWORD src1_sel:WORD_0
	v_or_b32_e32 v112, v112, v1
	buffer_load_dwordx4 v[48:51], v112, s[36:39], 0 offen
	v_lshlrev_b32_sdwa v113, s47, v8 dst_sel:DWORD dst_unused:UNUSED_PAD src0_sel:DWORD src1_sel:WORD_1
	v_or_b32_e32 v113, v113, v1
	buffer_load_dwordx4 v[52:55], v113, s[36:39], 0 offen
	v_lshlrev_b32_sdwa v112, s47, v9 dst_sel:DWORD dst_unused:UNUSED_PAD src0_sel:DWORD src1_sel:WORD_0
	v_or_b32_e32 v112, v112, v1
	buffer_load_dwordx4 v[56:59], v112, s[36:39], 0 offen
	v_lshlrev_b32_sdwa v113, s47, v9 dst_sel:DWORD dst_unused:UNUSED_PAD src0_sel:DWORD src1_sel:WORD_1
	v_or_b32_e32 v113, v113, v1
	buffer_load_dwordx4 v[60:63], v113, s[36:39], 0 offen
	v_lshlrev_b32_sdwa v112, s47, v10 dst_sel:DWORD dst_unused:UNUSED_PAD src0_sel:DWORD src1_sel:WORD_0
	v_or_b32_e32 v112, v112, v1
	buffer_load_dwordx4 v[64:67], v112, s[36:39], 0 offen
	v_lshlrev_b32_sdwa v113, s47, v10 dst_sel:DWORD dst_unused:UNUSED_PAD src0_sel:DWORD src1_sel:WORD_1
	v_or_b32_e32 v113, v113, v1
	buffer_load_dwordx4 v[68:71], v113, s[36:39], 0 offen
	v_lshlrev_b32_sdwa v112, s47, v11 dst_sel:DWORD dst_unused:UNUSED_PAD src0_sel:DWORD src1_sel:WORD_0
	v_or_b32_e32 v112, v112, v1
	buffer_load_dwordx4 v[72:75], v112, s[36:39], 0 offen
	v_lshlrev_b32_sdwa v113, s47, v11 dst_sel:DWORD dst_unused:UNUSED_PAD src0_sel:DWORD src1_sel:WORD_1
	v_or_b32_e32 v113, v113, v1
	buffer_load_dwordx4 v[76:79], v113, s[36:39], 0 offen
	v_lshlrev_b32_sdwa v112, s47, v12 dst_sel:DWORD dst_unused:UNUSED_PAD src0_sel:DWORD src1_sel:WORD_0
	v_or_b32_e32 v112, v112, v1
	buffer_load_dwordx4 v[80:83], v112, s[36:39], 0 offen
	v_lshlrev_b32_sdwa v113, s47, v12 dst_sel:DWORD dst_unused:UNUSED_PAD src0_sel:DWORD src1_sel:WORD_1
	v_or_b32_e32 v113, v113, v1
	buffer_load_dwordx4 v[84:87], v113, s[36:39], 0 offen
	v_lshlrev_b32_sdwa v112, s47, v13 dst_sel:DWORD dst_unused:UNUSED_PAD src0_sel:DWORD src1_sel:WORD_0
	v_or_b32_e32 v112, v112, v1
	buffer_load_dwordx4 v[88:91], v112, s[36:39], 0 offen
	v_lshlrev_b32_sdwa v113, s47, v13 dst_sel:DWORD dst_unused:UNUSED_PAD src0_sel:DWORD src1_sel:WORD_1
	v_or_b32_e32 v113, v113, v1
	buffer_load_dwordx4 v[92:95], v113, s[36:39], 0 offen
	v_lshlrev_b32_sdwa v112, s47, v14 dst_sel:DWORD dst_unused:UNUSED_PAD src0_sel:DWORD src1_sel:WORD_0
	v_or_b32_e32 v112, v112, v1
	buffer_load_dwordx4 v[96:99], v112, s[36:39], 0 offen
	v_lshlrev_b32_sdwa v113, s47, v14 dst_sel:DWORD dst_unused:UNUSED_PAD src0_sel:DWORD src1_sel:WORD_1
	v_or_b32_e32 v113, v113, v1
	buffer_load_dwordx4 v[100:103], v113, s[36:39], 0 offen
	v_lshlrev_b32_sdwa v112, s47, v15 dst_sel:DWORD dst_unused:UNUSED_PAD src0_sel:DWORD src1_sel:WORD_0
	v_or_b32_e32 v112, v112, v1
	buffer_load_dwordx4 v[104:107], v112, s[36:39], 0 offen
	v_lshlrev_b32_sdwa v113, s47, v15 dst_sel:DWORD dst_unused:UNUSED_PAD src0_sel:DWORD src1_sel:WORD_1
	v_or_b32_e32 v113, v113, v1
	buffer_load_dwordx4 v[108:111], v113, s[36:39], 0 offen
	global_load_dword v252, v5, s[28:29]

.Lv_got_l0:
	s_lshl_b32 s2, s22, 8
	s_add_u32 s2, s28, s2
	s_addc_u32 s3, s29, 0
	global_load_dwordx4 v[8:11], v2, s[2:3]
	global_load_dwordx4 v[12:15], v2, s[2:3] offset:16
	s_lshl_b32 s2, s21, 8
	s_add_u32 s2, s30, s2
	s_addc_u32 s3, s31, 0
	global_load_dwordx4 v[32:35], v2, s[2:3]
	global_load_dwordx4 v[36:39], v2, s[2:3] offset:16
	s_waitcnt vmcnt(20)
	v_cvt_pk_f32_fp8_e32 v[116:117], v48
	v_cvt_pk_f32_fp8_sdwa v[118:119], v48 src0_sel:WORD_1
	v_cvt_pk_f32_fp8_e32 v[120:121], v49
	v_cvt_pk_f32_fp8_sdwa v[122:123], v49 src0_sel:WORD_1
	v_cvt_pk_f32_fp8_e32 v[124:125], v50
	v_cvt_pk_f32_fp8_sdwa v[126:127], v50 src0_sel:WORD_1
	v_cvt_pk_f32_fp8_e32 v[128:129], v51
	v_cvt_pk_f32_fp8_sdwa v[130:131], v51 src0_sel:WORD_1
	v_lshlrev_b32_e32 v148, 16, v24
	v_lshlrev_b32_sdwa v112, s47, v16 dst_sel:DWORD dst_unused:UNUSED_PAD src0_sel:DWORD src1_sel:WORD_0
	v_or_b32_e32 v112, v112, v1
	buffer_load_dwordx4 v[48:51], v112, s[36:39], 0 offen
	v_pk_mul_f32 v[152:153], v[148:149], v[116:117] op_sel_hi:[0,1]
	v_pk_mul_f32 v[154:155], v[148:149], v[118:119] op_sel_hi:[0,1]
	v_pk_mul_f32 v[156:157], v[148:149], v[120:121] op_sel_hi:[0,1]
	v_pk_mul_f32 v[158:159], v[148:149], v[122:123] op_sel_hi:[0,1]
	v_pk_mul_f32 v[160:161], v[148:149], v[124:125] op_sel_hi:[0,1]
	v_pk_mul_f32 v[162:163], v[148:149], v[126:127] op_sel_hi:[0,1]
	v_pk_mul_f32 v[164:165], v[148:149], v[128:129] op_sel_hi:[0,1]
	v_pk_mul_f32 v[166:167], v[148:149], v[130:131] op_sel_hi:[0,1]
	s_waitcnt vmcnt(20)
	v_cvt_pk_f32_fp8_e32 v[132:133], v52
	v_cvt_pk_f32_fp8_sdwa v[134:135], v52 src0_sel:WORD_1
	v_cvt_pk_f32_fp8_e32 v[136:137], v53
	v_cvt_pk_f32_fp8_sdwa v[138:139], v53 src0_sel:WORD_1
	v_cvt_pk_f32_fp8_e32 v[140:141], v54
	v_cvt_pk_f32_fp8_sdwa v[142:143], v54 src0_sel:WORD_1
	v_cvt_pk_f32_fp8_e32 v[144:145], v55
	v_cvt_pk_f32_fp8_sdwa v[146:147], v55 src0_sel:WORD_1
	v_and_b32_e32 v150, 0xffff0000, v24
	v_lshlrev_b32_sdwa v113, s47, v16 dst_sel:DWORD dst_unused:UNUSED_PAD src0_sel:DWORD src1_sel:WORD_1
	v_or_b32_e32 v113, v113, v1
	buffer_load_dwordx4 v[52:55], v113, s[36:39], 0 offen
	v_pk_fma_f32 v[152:153], v[150:151], v[132:133], v[152:153] op_sel_hi:[0,1,1]
	v_pk_fma_f32 v[154:155], v[150:151], v[134:135], v[154:155] op_sel_hi:[0,1,1]
	v_pk_fma_f32 v[156:157], v[150:151], v[136:137], v[156:157] op_sel_hi:[0,1,1]
	v_pk_fma_f32 v[158:159], v[150:151], v[138:139], v[158:159] op_sel_hi:[0,1,1]
	v_pk_fma_f32 v[160:161], v[150:151], v[140:141], v[160:161] op_sel_hi:[0,1,1]
	v_pk_fma_f32 v[162:163], v[150:151], v[142:143], v[162:163] op_sel_hi:[0,1,1]
	v_pk_fma_f32 v[164:165], v[150:151], v[144:145], v[164:165] op_sel_hi:[0,1,1]
	v_pk_fma_f32 v[166:167], v[150:151], v[146:147], v[166:167] op_sel_hi:[0,1,1]
	s_waitcnt vmcnt(20)
	v_cvt_pk_f32_fp8_e32 v[116:117], v56
	v_cvt_pk_f32_fp8_sdwa v[118:119], v56 src0_sel:WORD_1
	v_cvt_pk_f32_fp8_e32 v[120:121], v57
	v_cvt_pk_f32_fp8_sdwa v[122:123], v57 src0_sel:WORD_1
	v_cvt_pk_f32_fp8_e32 v[124:125], v58
	v_cvt_pk_f32_fp8_sdwa v[126:127], v58 src0_sel:WORD_1
	v_cvt_pk_f32_fp8_e32 v[128:129], v59
	v_cvt_pk_f32_fp8_sdwa v[130:131], v59 src0_sel:WORD_1
	v_lshlrev_b32_e32 v148, 16, v25
	v_lshlrev_b32_sdwa v112, s47, v17 dst_sel:DWORD dst_unused:UNUSED_PAD src0_sel:DWORD src1_sel:WORD_0
	v_or_b32_e32 v112, v112, v1
	buffer_load_dwordx4 v[56:59], v112, s[36:39], 0 offen
	v_pk_fma_f32 v[152:153], v[148:149], v[116:117], v[152:153] op_sel_hi:[0,1,1]
	v_pk_fma_f32 v[154:155], v[148:149], v[118:119], v[154:155] op_sel_hi:[0,1,1]
	v_pk_fma_f32 v[156:157], v[148:149], v[120:121], v[156:157] op_sel_hi:[0,1,1]
	v_pk_fma_f32 v[158:159], v[148:149], v[122:123], v[158:159] op_sel_hi:[0,1,1]
	v_pk_fma_f32 v[160:161], v[148:149], v[124:125], v[160:161] op_sel_hi:[0,1,1]
	v_pk_fma_f32 v[162:163], v[148:149], v[126:127], v[162:163] op_sel_hi:[0,1,1]
	v_pk_fma_f32 v[164:165], v[148:149], v[128:129], v[164:165] op_sel_hi:[0,1,1]
	v_pk_fma_f32 v[166:167], v[148:149], v[130:131], v[166:167] op_sel_hi:[0,1,1]
	s_waitcnt vmcnt(20)
	v_cvt_pk_f32_fp8_e32 v[132:133], v60
	v_cvt_pk_f32_fp8_sdwa v[134:135], v60 src0_sel:WORD_1
	v_cvt_pk_f32_fp8_e32 v[136:137], v61
	v_cvt_pk_f32_fp8_sdwa v[138:139], v61 src0_sel:WORD_1
	v_cvt_pk_f32_fp8_e32 v[140:141], v62
	v_cvt_pk_f32_fp8_sdwa v[142:143], v62 src0_sel:WORD_1
	v_cvt_pk_f32_fp8_e32 v[144:145], v63
	v_cvt_pk_f32_fp8_sdwa v[146:147], v63 src0_sel:WORD_1
	v_and_b32_e32 v150, 0xffff0000, v25
	v_lshlrev_b32_sdwa v113, s47, v17 dst_sel:DWORD dst_unused:UNUSED_PAD src0_sel:DWORD src1_sel:WORD_1
	v_or_b32_e32 v113, v113, v1
	buffer_load_dwordx4 v[60:63], v113, s[36:39], 0 offen
	v_pk_fma_f32 v[152:153], v[150:151], v[132:133], v[152:153] op_sel_hi:[0,1,1]
	v_pk_fma_f32 v[154:155], v[150:151], v[134:135], v[154:155] op_sel_hi:[0,1,1]
	v_pk_fma_f32 v[156:157], v[150:151], v[136:137], v[156:157] op_sel_hi:[0,1,1]
	v_pk_fma_f32 v[158:159], v[150:151], v[138:139], v[158:159] op_sel_hi:[0,1,1]
	v_pk_fma_f32 v[160:161], v[150:151], v[140:141], v[160:161] op_sel_hi:[0,1,1]
	v_pk_fma_f32 v[162:163], v[150:151], v[142:143], v[162:163] op_sel_hi:[0,1,1]
	v_pk_fma_f32 v[164:165], v[150:151], v[144:145], v[164:165] op_sel_hi:[0,1,1]
	v_pk_fma_f32 v[166:167], v[150:151], v[146:147], v[166:167] op_sel_hi:[0,1,1]
	s_waitcnt vmcnt(20)
	v_cvt_pk_f32_fp8_e32 v[116:117], v64
	v_cvt_pk_f32_fp8_sdwa v[118:119], v64 src0_sel:WORD_1
	v_cvt_pk_f32_fp8_e32 v[120:121], v65
	v_cvt_pk_f32_fp8_sdwa v[122:123], v65 src0_sel:WORD_1
	v_cvt_pk_f32_fp8_e32 v[124:125], v66
	v_cvt_pk_f32_fp8_sdwa v[126:127], v66 src0_sel:WORD_1
	v_cvt_pk_f32_fp8_e32 v[128:129], v67
	v_cvt_pk_f32_fp8_sdwa v[130:131], v67 src0_sel:WORD_1
	v_lshlrev_b32_e32 v148, 16, v26
	v_lshlrev_b32_sdwa v112, s47, v18 dst_sel:DWORD dst_unused:UNUSED_PAD src0_sel:DWORD src1_sel:WORD_0
	v_or_b32_e32 v112, v112, v1
	buffer_load_dwordx4 v[64:67], v112, s[36:39], 0 offen
	v_pk_fma_f32 v[152:153], v[148:149], v[116:117], v[152:153] op_sel_hi:[0,1,1]
	v_pk_fma_f32 v[154:155], v[148:149], v[118:119], v[154:155] op_sel_hi:[0,1,1]
	v_pk_fma_f32 v[156:157], v[148:149], v[120:121], v[156:157] op_sel_hi:[0,1,1]
	v_pk_fma_f32 v[158:159], v[148:149], v[122:123], v[158:159] op_sel_hi:[0,1,1]
	v_pk_fma_f32 v[160:161], v[148:149], v[124:125], v[160:161] op_sel_hi:[0,1,1]
	v_pk_fma_f32 v[162:163], v[148:149], v[126:127], v[162:163] op_sel_hi:[0,1,1]
	v_pk_fma_f32 v[164:165], v[148:149], v[128:129], v[164:165] op_sel_hi:[0,1,1]
	v_pk_fma_f32 v[166:167], v[148:149], v[130:131], v[166:167] op_sel_hi:[0,1,1]
	s_waitcnt vmcnt(20)
	v_cvt_pk_f32_fp8_e32 v[132:133], v68
	v_cvt_pk_f32_fp8_sdwa v[134:135], v68 src0_sel:WORD_1
	v_cvt_pk_f32_fp8_e32 v[136:137], v69
	v_cvt_pk_f32_fp8_sdwa v[138:139], v69 src0_sel:WORD_1
	v_cvt_pk_f32_fp8_e32 v[140:141], v70
	v_cvt_pk_f32_fp8_sdwa v[142:143], v70 src0_sel:WORD_1
	v_cvt_pk_f32_fp8_e32 v[144:145], v71
	v_cvt_pk_f32_fp8_sdwa v[146:147], v71 src0_sel:WORD_1
	v_and_b32_e32 v150, 0xffff0000, v26
	v_lshlrev_b32_sdwa v113, s47, v18 dst_sel:DWORD dst_unused:UNUSED_PAD src0_sel:DWORD src1_sel:WORD_1
	v_or_b32_e32 v113, v113, v1
	buffer_load_dwordx4 v[68:71], v113, s[36:39], 0 offen
	v_pk_fma_f32 v[152:153], v[150:151], v[132:133], v[152:153] op_sel_hi:[0,1,1]
	v_pk_fma_f32 v[154:155], v[150:151], v[134:135], v[154:155] op_sel_hi:[0,1,1]
	v_pk_fma_f32 v[156:157], v[150:151], v[136:137], v[156:157] op_sel_hi:[0,1,1]
	v_pk_fma_f32 v[158:159], v[150:151], v[138:139], v[158:159] op_sel_hi:[0,1,1]
	v_pk_fma_f32 v[160:161], v[150:151], v[140:141], v[160:161] op_sel_hi:[0,1,1]
	v_pk_fma_f32 v[162:163], v[150:151], v[142:143], v[162:163] op_sel_hi:[0,1,1]
	v_pk_fma_f32 v[164:165], v[150:151], v[144:145], v[164:165] op_sel_hi:[0,1,1]
	v_pk_fma_f32 v[166:167], v[150:151], v[146:147], v[166:167] op_sel_hi:[0,1,1]
	s_waitcnt vmcnt(20)
	v_cvt_pk_f32_fp8_e32 v[116:117], v72
	v_cvt_pk_f32_fp8_sdwa v[118:119], v72 src0_sel:WORD_1
	v_cvt_pk_f32_fp8_e32 v[120:121], v73
	v_cvt_pk_f32_fp8_sdwa v[122:123], v73 src0_sel:WORD_1
	v_cvt_pk_f32_fp8_e32 v[124:125], v74
	v_cvt_pk_f32_fp8_sdwa v[126:127], v74 src0_sel:WORD_1
	v_cvt_pk_f32_fp8_e32 v[128:129], v75
	v_cvt_pk_f32_fp8_sdwa v[130:131], v75 src0_sel:WORD_1
	v_lshlrev_b32_e32 v148, 16, v27
	v_lshlrev_b32_sdwa v112, s47, v19 dst_sel:DWORD dst_unused:UNUSED_PAD src0_sel:DWORD src1_sel:WORD_0
	v_or_b32_e32 v112, v112, v1
	buffer_load_dwordx4 v[72:75], v112, s[36:39], 0 offen
	v_pk_fma_f32 v[152:153], v[148:149], v[116:117], v[152:153] op_sel_hi:[0,1,1]
	v_pk_fma_f32 v[154:155], v[148:149], v[118:119], v[154:155] op_sel_hi:[0,1,1]
	v_pk_fma_f32 v[156:157], v[148:149], v[120:121], v[156:157] op_sel_hi:[0,1,1]
	v_pk_fma_f32 v[158:159], v[148:149], v[122:123], v[158:159] op_sel_hi:[0,1,1]
	v_pk_fma_f32 v[160:161], v[148:149], v[124:125], v[160:161] op_sel_hi:[0,1,1]
	v_pk_fma_f32 v[162:163], v[148:149], v[126:127], v[162:163] op_sel_hi:[0,1,1]
	v_pk_fma_f32 v[164:165], v[148:149], v[128:129], v[164:165] op_sel_hi:[0,1,1]
	v_pk_fma_f32 v[166:167], v[148:149], v[130:131], v[166:167] op_sel_hi:[0,1,1]
	s_waitcnt vmcnt(20)
	v_cvt_pk_f32_fp8_e32 v[132:133], v76
	v_cvt_pk_f32_fp8_sdwa v[134:135], v76 src0_sel:WORD_1
	v_cvt_pk_f32_fp8_e32 v[136:137], v77
	v_cvt_pk_f32_fp8_sdwa v[138:139], v77 src0_sel:WORD_1
	v_cvt_pk_f32_fp8_e32 v[140:141], v78
	v_cvt_pk_f32_fp8_sdwa v[142:143], v78 src0_sel:WORD_1
	v_cvt_pk_f32_fp8_e32 v[144:145], v79
	v_cvt_pk_f32_fp8_sdwa v[146:147], v79 src0_sel:WORD_1
	v_and_b32_e32 v150, 0xffff0000, v27
	v_lshlrev_b32_sdwa v113, s47, v19 dst_sel:DWORD dst_unused:UNUSED_PAD src0_sel:DWORD src1_sel:WORD_1
	v_or_b32_e32 v113, v113, v1
	buffer_load_dwordx4 v[76:79], v113, s[36:39], 0 offen
	v_pk_fma_f32 v[152:153], v[150:151], v[132:133], v[152:153] op_sel_hi:[0,1,1]
	v_pk_fma_f32 v[154:155], v[150:151], v[134:135], v[154:155] op_sel_hi:[0,1,1]
	v_pk_fma_f32 v[156:157], v[150:151], v[136:137], v[156:157] op_sel_hi:[0,1,1]
	v_pk_fma_f32 v[158:159], v[150:151], v[138:139], v[158:159] op_sel_hi:[0,1,1]
	v_pk_fma_f32 v[160:161], v[150:151], v[140:141], v[160:161] op_sel_hi:[0,1,1]
	v_pk_fma_f32 v[162:163], v[150:151], v[142:143], v[162:163] op_sel_hi:[0,1,1]
	v_pk_fma_f32 v[164:165], v[150:151], v[144:145], v[164:165] op_sel_hi:[0,1,1]
	v_pk_fma_f32 v[166:167], v[150:151], v[146:147], v[166:167] op_sel_hi:[0,1,1]
	s_waitcnt vmcnt(20)
	v_cvt_pk_f32_fp8_e32 v[116:117], v80
	v_cvt_pk_f32_fp8_sdwa v[118:119], v80 src0_sel:WORD_1
	v_cvt_pk_f32_fp8_e32 v[120:121], v81
	v_cvt_pk_f32_fp8_sdwa v[122:123], v81 src0_sel:WORD_1
	v_cvt_pk_f32_fp8_e32 v[124:125], v82
	v_cvt_pk_f32_fp8_sdwa v[126:127], v82 src0_sel:WORD_1
	v_cvt_pk_f32_fp8_e32 v[128:129], v83
	v_cvt_pk_f32_fp8_sdwa v[130:131], v83 src0_sel:WORD_1
	v_lshlrev_b32_e32 v148, 16, v28
	v_lshlrev_b32_sdwa v112, s47, v20 dst_sel:DWORD dst_unused:UNUSED_PAD src0_sel:DWORD src1_sel:WORD_0
	v_or_b32_e32 v112, v112, v1
	buffer_load_dwordx4 v[80:83], v112, s[36:39], 0 offen
	v_pk_fma_f32 v[152:153], v[148:149], v[116:117], v[152:153] op_sel_hi:[0,1,1]
	v_pk_fma_f32 v[154:155], v[148:149], v[118:119], v[154:155] op_sel_hi:[0,1,1]
	v_pk_fma_f32 v[156:157], v[148:149], v[120:121], v[156:157] op_sel_hi:[0,1,1]
	v_pk_fma_f32 v[158:159], v[148:149], v[122:123], v[158:159] op_sel_hi:[0,1,1]
	v_pk_fma_f32 v[160:161], v[148:149], v[124:125], v[160:161] op_sel_hi:[0,1,1]
	v_pk_fma_f32 v[162:163], v[148:149], v[126:127], v[162:163] op_sel_hi:[0,1,1]
	v_pk_fma_f32 v[164:165], v[148:149], v[128:129], v[164:165] op_sel_hi:[0,1,1]
	v_pk_fma_f32 v[166:167], v[148:149], v[130:131], v[166:167] op_sel_hi:[0,1,1]
	s_waitcnt vmcnt(20)
	v_cvt_pk_f32_fp8_e32 v[132:133], v84
	v_cvt_pk_f32_fp8_sdwa v[134:135], v84 src0_sel:WORD_1
	v_cvt_pk_f32_fp8_e32 v[136:137], v85
	v_cvt_pk_f32_fp8_sdwa v[138:139], v85 src0_sel:WORD_1
	v_cvt_pk_f32_fp8_e32 v[140:141], v86
	v_cvt_pk_f32_fp8_sdwa v[142:143], v86 src0_sel:WORD_1
	v_cvt_pk_f32_fp8_e32 v[144:145], v87
	v_cvt_pk_f32_fp8_sdwa v[146:147], v87 src0_sel:WORD_1
	v_and_b32_e32 v150, 0xffff0000, v28
	v_lshlrev_b32_sdwa v113, s47, v20 dst_sel:DWORD dst_unused:UNUSED_PAD src0_sel:DWORD src1_sel:WORD_1
	v_or_b32_e32 v113, v113, v1
	buffer_load_dwordx4 v[84:87], v113, s[36:39], 0 offen
	v_pk_fma_f32 v[152:153], v[150:151], v[132:133], v[152:153] op_sel_hi:[0,1,1]
	v_pk_fma_f32 v[154:155], v[150:151], v[134:135], v[154:155] op_sel_hi:[0,1,1]
	v_pk_fma_f32 v[156:157], v[150:151], v[136:137], v[156:157] op_sel_hi:[0,1,1]
	v_pk_fma_f32 v[158:159], v[150:151], v[138:139], v[158:159] op_sel_hi:[0,1,1]
	v_pk_fma_f32 v[160:161], v[150:151], v[140:141], v[160:161] op_sel_hi:[0,1,1]
	v_pk_fma_f32 v[162:163], v[150:151], v[142:143], v[162:163] op_sel_hi:[0,1,1]
	v_pk_fma_f32 v[164:165], v[150:151], v[144:145], v[164:165] op_sel_hi:[0,1,1]
	v_pk_fma_f32 v[166:167], v[150:151], v[146:147], v[166:167] op_sel_hi:[0,1,1]
	s_waitcnt vmcnt(20)
	v_cvt_pk_f32_fp8_e32 v[116:117], v88
	v_cvt_pk_f32_fp8_sdwa v[118:119], v88 src0_sel:WORD_1
	v_cvt_pk_f32_fp8_e32 v[120:121], v89
	v_cvt_pk_f32_fp8_sdwa v[122:123], v89 src0_sel:WORD_1
	v_cvt_pk_f32_fp8_e32 v[124:125], v90
	v_cvt_pk_f32_fp8_sdwa v[126:127], v90 src0_sel:WORD_1
	v_cvt_pk_f32_fp8_e32 v[128:129], v91
	v_cvt_pk_f32_fp8_sdwa v[130:131], v91 src0_sel:WORD_1
	v_lshlrev_b32_e32 v148, 16, v29
	v_lshlrev_b32_sdwa v112, s47, v21 dst_sel:DWORD dst_unused:UNUSED_PAD src0_sel:DWORD src1_sel:WORD_0
	v_or_b32_e32 v112, v112, v1
	buffer_load_dwordx4 v[88:91], v112, s[36:39], 0 offen
	v_pk_fma_f32 v[152:153], v[148:149], v[116:117], v[152:153] op_sel_hi:[0,1,1]
	v_pk_fma_f32 v[154:155], v[148:149], v[118:119], v[154:155] op_sel_hi:[0,1,1]
	v_pk_fma_f32 v[156:157], v[148:149], v[120:121], v[156:157] op_sel_hi:[0,1,1]
	v_pk_fma_f32 v[158:159], v[148:149], v[122:123], v[158:159] op_sel_hi:[0,1,1]
	v_pk_fma_f32 v[160:161], v[148:149], v[124:125], v[160:161] op_sel_hi:[0,1,1]
	v_pk_fma_f32 v[162:163], v[148:149], v[126:127], v[162:163] op_sel_hi:[0,1,1]
	v_pk_fma_f32 v[164:165], v[148:149], v[128:129], v[164:165] op_sel_hi:[0,1,1]
	v_pk_fma_f32 v[166:167], v[148:149], v[130:131], v[166:167] op_sel_hi:[0,1,1]
	s_waitcnt vmcnt(20)
	v_cvt_pk_f32_fp8_e32 v[132:133], v92
	v_cvt_pk_f32_fp8_sdwa v[134:135], v92 src0_sel:WORD_1
	v_cvt_pk_f32_fp8_e32 v[136:137], v93
	v_cvt_pk_f32_fp8_sdwa v[138:139], v93 src0_sel:WORD_1
	v_cvt_pk_f32_fp8_e32 v[140:141], v94
	v_cvt_pk_f32_fp8_sdwa v[142:143], v94 src0_sel:WORD_1
	v_cvt_pk_f32_fp8_e32 v[144:145], v95
	v_cvt_pk_f32_fp8_sdwa v[146:147], v95 src0_sel:WORD_1
	v_and_b32_e32 v150, 0xffff0000, v29
	v_lshlrev_b32_sdwa v113, s47, v21 dst_sel:DWORD dst_unused:UNUSED_PAD src0_sel:DWORD src1_sel:WORD_1
	v_or_b32_e32 v113, v113, v1
	buffer_load_dwordx4 v[92:95], v113, s[36:39], 0 offen
	v_pk_fma_f32 v[152:153], v[150:151], v[132:133], v[152:153] op_sel_hi:[0,1,1]
	v_pk_fma_f32 v[154:155], v[150:151], v[134:135], v[154:155] op_sel_hi:[0,1,1]
	v_pk_fma_f32 v[156:157], v[150:151], v[136:137], v[156:157] op_sel_hi:[0,1,1]
	v_pk_fma_f32 v[158:159], v[150:151], v[138:139], v[158:159] op_sel_hi:[0,1,1]
	v_pk_fma_f32 v[160:161], v[150:151], v[140:141], v[160:161] op_sel_hi:[0,1,1]
	v_pk_fma_f32 v[162:163], v[150:151], v[142:143], v[162:163] op_sel_hi:[0,1,1]
	v_pk_fma_f32 v[164:165], v[150:151], v[144:145], v[164:165] op_sel_hi:[0,1,1]
	v_pk_fma_f32 v[166:167], v[150:151], v[146:147], v[166:167] op_sel_hi:[0,1,1]
	s_waitcnt vmcnt(20)
	v_cvt_pk_f32_fp8_e32 v[116:117], v96
	v_cvt_pk_f32_fp8_sdwa v[118:119], v96 src0_sel:WORD_1
	v_cvt_pk_f32_fp8_e32 v[120:121], v97
	v_cvt_pk_f32_fp8_sdwa v[122:123], v97 src0_sel:WORD_1
	v_cvt_pk_f32_fp8_e32 v[124:125], v98
	v_cvt_pk_f32_fp8_sdwa v[126:127], v98 src0_sel:WORD_1
	v_cvt_pk_f32_fp8_e32 v[128:129], v99
	v_cvt_pk_f32_fp8_sdwa v[130:131], v99 src0_sel:WORD_1
	v_lshlrev_b32_e32 v148, 16, v30
	v_lshlrev_b32_sdwa v112, s47, v22 dst_sel:DWORD dst_unused:UNUSED_PAD src0_sel:DWORD src1_sel:WORD_0
	v_or_b32_e32 v112, v112, v1
	buffer_load_dwordx4 v[96:99], v112, s[36:39], 0 offen
	v_pk_fma_f32 v[152:153], v[148:149], v[116:117], v[152:153] op_sel_hi:[0,1,1]
	v_pk_fma_f32 v[154:155], v[148:149], v[118:119], v[154:155] op_sel_hi:[0,1,1]
	v_pk_fma_f32 v[156:157], v[148:149], v[120:121], v[156:157] op_sel_hi:[0,1,1]
	v_pk_fma_f32 v[158:159], v[148:149], v[122:123], v[158:159] op_sel_hi:[0,1,1]
	v_pk_fma_f32 v[160:161], v[148:149], v[124:125], v[160:161] op_sel_hi:[0,1,1]
	v_pk_fma_f32 v[162:163], v[148:149], v[126:127], v[162:163] op_sel_hi:[0,1,1]
	v_pk_fma_f32 v[164:165], v[148:149], v[128:129], v[164:165] op_sel_hi:[0,1,1]
	v_pk_fma_f32 v[166:167], v[148:149], v[130:131], v[166:167] op_sel_hi:[0,1,1]
	s_waitcnt vmcnt(20)
	v_cvt_pk_f32_fp8_e32 v[132:133], v100
	v_cvt_pk_f32_fp8_sdwa v[134:135], v100 src0_sel:WORD_1
	v_cvt_pk_f32_fp8_e32 v[136:137], v101
	v_cvt_pk_f32_fp8_sdwa v[138:139], v101 src0_sel:WORD_1
	v_cvt_pk_f32_fp8_e32 v[140:141], v102
	v_cvt_pk_f32_fp8_sdwa v[142:143], v102 src0_sel:WORD_1
	v_cvt_pk_f32_fp8_e32 v[144:145], v103
	v_cvt_pk_f32_fp8_sdwa v[146:147], v103 src0_sel:WORD_1
	v_and_b32_e32 v150, 0xffff0000, v30
	v_lshlrev_b32_sdwa v113, s47, v22 dst_sel:DWORD dst_unused:UNUSED_PAD src0_sel:DWORD src1_sel:WORD_1
	v_or_b32_e32 v113, v113, v1
	buffer_load_dwordx4 v[100:103], v113, s[36:39], 0 offen
	v_pk_fma_f32 v[152:153], v[150:151], v[132:133], v[152:153] op_sel_hi:[0,1,1]
	v_pk_fma_f32 v[154:155], v[150:151], v[134:135], v[154:155] op_sel_hi:[0,1,1]
	v_pk_fma_f32 v[156:157], v[150:151], v[136:137], v[156:157] op_sel_hi:[0,1,1]
	v_pk_fma_f32 v[158:159], v[150:151], v[138:139], v[158:159] op_sel_hi:[0,1,1]
	v_pk_fma_f32 v[160:161], v[150:151], v[140:141], v[160:161] op_sel_hi:[0,1,1]
	v_pk_fma_f32 v[162:163], v[150:151], v[142:143], v[162:163] op_sel_hi:[0,1,1]
	v_pk_fma_f32 v[164:165], v[150:151], v[144:145], v[164:165] op_sel_hi:[0,1,1]
	v_pk_fma_f32 v[166:167], v[150:151], v[146:147], v[166:167] op_sel_hi:[0,1,1]
	s_waitcnt vmcnt(20)
	v_cvt_pk_f32_fp8_e32 v[116:117], v104
	v_cvt_pk_f32_fp8_sdwa v[118:119], v104 src0_sel:WORD_1
	v_cvt_pk_f32_fp8_e32 v[120:121], v105
	v_cvt_pk_f32_fp8_sdwa v[122:123], v105 src0_sel:WORD_1
	v_cvt_pk_f32_fp8_e32 v[124:125], v106
	v_cvt_pk_f32_fp8_sdwa v[126:127], v106 src0_sel:WORD_1
	v_cvt_pk_f32_fp8_e32 v[128:129], v107
	v_cvt_pk_f32_fp8_sdwa v[130:131], v107 src0_sel:WORD_1
	v_lshlrev_b32_e32 v148, 16, v31
	v_lshlrev_b32_sdwa v112, s47, v23 dst_sel:DWORD dst_unused:UNUSED_PAD src0_sel:DWORD src1_sel:WORD_0
	v_or_b32_e32 v112, v112, v1
	buffer_load_dwordx4 v[104:107], v112, s[36:39], 0 offen
	v_pk_fma_f32 v[152:153], v[148:149], v[116:117], v[152:153] op_sel_hi:[0,1,1]
	v_pk_fma_f32 v[154:155], v[148:149], v[118:119], v[154:155] op_sel_hi:[0,1,1]
	v_pk_fma_f32 v[156:157], v[148:149], v[120:121], v[156:157] op_sel_hi:[0,1,1]
	v_pk_fma_f32 v[158:159], v[148:149], v[122:123], v[158:159] op_sel_hi:[0,1,1]
	v_pk_fma_f32 v[160:161], v[148:149], v[124:125], v[160:161] op_sel_hi:[0,1,1]
	v_pk_fma_f32 v[162:163], v[148:149], v[126:127], v[162:163] op_sel_hi:[0,1,1]
	v_pk_fma_f32 v[164:165], v[148:149], v[128:129], v[164:165] op_sel_hi:[0,1,1]
	v_pk_fma_f32 v[166:167], v[148:149], v[130:131], v[166:167] op_sel_hi:[0,1,1]
	s_waitcnt vmcnt(20)
	v_cvt_pk_f32_fp8_e32 v[132:133], v108
	v_cvt_pk_f32_fp8_sdwa v[134:135], v108 src0_sel:WORD_1
	v_cvt_pk_f32_fp8_e32 v[136:137], v109
	v_cvt_pk_f32_fp8_sdwa v[138:139], v109 src0_sel:WORD_1
	v_cvt_pk_f32_fp8_e32 v[140:141], v110
	v_cvt_pk_f32_fp8_sdwa v[142:143], v110 src0_sel:WORD_1
	v_cvt_pk_f32_fp8_e32 v[144:145], v111
	v_cvt_pk_f32_fp8_sdwa v[146:147], v111 src0_sel:WORD_1
	v_and_b32_e32 v150, 0xffff0000, v31
	v_lshlrev_b32_sdwa v113, s47, v23 dst_sel:DWORD dst_unused:UNUSED_PAD src0_sel:DWORD src1_sel:WORD_1
	v_or_b32_e32 v113, v113, v1
	buffer_load_dwordx4 v[108:111], v113, s[36:39], 0 offen
	v_pk_fma_f32 v[152:153], v[150:151], v[132:133], v[152:153] op_sel_hi:[0,1,1]
	v_pk_fma_f32 v[154:155], v[150:151], v[134:135], v[154:155] op_sel_hi:[0,1,1]
	v_pk_fma_f32 v[156:157], v[150:151], v[136:137], v[156:157] op_sel_hi:[0,1,1]
	v_pk_fma_f32 v[158:159], v[150:151], v[138:139], v[158:159] op_sel_hi:[0,1,1]
	v_pk_fma_f32 v[160:161], v[150:151], v[140:141], v[160:161] op_sel_hi:[0,1,1]
	v_pk_fma_f32 v[162:163], v[150:151], v[142:143], v[162:163] op_sel_hi:[0,1,1]
	v_pk_fma_f32 v[164:165], v[150:151], v[144:145], v[164:165] op_sel_hi:[0,1,1]
	v_pk_fma_f32 v[166:167], v[150:151], v[146:147], v[166:167] op_sel_hi:[0,1,1]
	s_nop 1
	v_permlane32_swap_b32_e32 v152, v160
	v_permlane32_swap_b32_e32 v153, v161
	v_permlane32_swap_b32_e32 v154, v162
	v_permlane32_swap_b32_e32 v155, v163
	v_permlane32_swap_b32_e32 v156, v164
	v_permlane32_swap_b32_e32 v157, v165
	v_permlane32_swap_b32_e32 v158, v166
	v_permlane32_swap_b32_e32 v159, v167
	v_add_f32_e32 v168, v152, v160
	v_add_f32_e32 v169, v153, v161
	v_add_f32_e32 v170, v154, v162
	v_add_f32_e32 v171, v155, v163
	v_add_f32_e32 v172, v156, v164
	v_add_f32_e32 v173, v157, v165
	v_add_f32_e32 v174, v158, v166
	v_add_f32_e32 v175, v159, v167
	s_nop 1
	v_permlane16_swap_b32_e32 v168, v172
	v_permlane16_swap_b32_e32 v169, v173
	v_permlane16_swap_b32_e32 v170, v174
	v_permlane16_swap_b32_e32 v171, v175
	v_add_f32_e32 v176, v168, v172
	v_add_f32_e32 v177, v169, v173
	v_add_f32_e32 v178, v170, v174
	v_add_f32_e32 v179, v171, v175
	v_cndmask_b32_e64 v180, v176, v178, s[44:45]
	v_cndmask_b32_e64 v181, v177, v179, s[44:45]
	v_cndmask_b32_e64 v182, v178, v176, s[44:45]
	v_cndmask_b32_e64 v183, v179, v177, s[44:45]
	s_nop 0
	v_add_f32_dpp v184, v180, v182 row_ror:8 row_mask:0xf bank_mask:0xf
	v_add_f32_dpp v185, v181, v183 row_ror:8 row_mask:0xf bank_mask:0xf
	v_cvt_pk_bf16_f32 v186, v184, v185
	s_lshl_b32 s2, s20, 12
	s_add_u32 s2, s34, s2
	s_addc_u32 s3, s35, 0
	global_store_dword v3, v186, s[2:3]
	s_mov_b32 s20, s21
	s_mov_b32 s48, s49
	s_mov_b32 s21, s22
	s_mov_b32 s49, s50
	s_cmp_eq_u32 s48, 0
	s_cbranch_scc1 .Lv_drain
	s_cmp_lg_u32 s26, 32
	s_cbranch_scc1 .Lv_norot_l1
	v_readfirstlane_b32 s23, v6
	s_mov_b64 exec, 1
	global_atomic_inc v6, v5, v7, s[6:7] sc0
	s_mov_b64 exec, -1
	s_mov_b32 s26, 0

.Lv_got_l1:
	s_lshl_b32 s2, s22, 8
	s_add_u32 s2, s28, s2
	s_addc_u32 s3, s29, 0
	global_load_dwordx4 v[16:19], v2, s[2:3]
	global_load_dwordx4 v[20:23], v2, s[2:3] offset:16
	s_lshl_b32 s2, s21, 8
	s_add_u32 s2, s30, s2
	s_addc_u32 s3, s31, 0
	global_load_dwordx4 v[24:27], v2, s[2:3]
	global_load_dwordx4 v[28:31], v2, s[2:3] offset:16
	s_waitcnt vmcnt(20)
	v_cvt_pk_f32_fp8_e32 v[116:117], v48
	v_cvt_pk_f32_fp8_sdwa v[118:119], v48 src0_sel:WORD_1
	v_cvt_pk_f32_fp8_e32 v[120:121], v49
	v_cvt_pk_f32_fp8_sdwa v[122:123], v49 src0_sel:WORD_1
	v_cvt_pk_f32_fp8_e32 v[124:125], v50
	v_cvt_pk_f32_fp8_sdwa v[126:127], v50 src0_sel:WORD_1
	v_cvt_pk_f32_fp8_e32 v[128:129], v51
	v_cvt_pk_f32_fp8_sdwa v[130:131], v51 src0_sel:WORD_1
	v_lshlrev_b32_e32 v148, 16, v32
	v_lshlrev_b32_sdwa v112, s47, v8 dst_sel:DWORD dst_unused:UNUSED_PAD src0_sel:DWORD src1_sel:WORD_0
	v_or_b32_e32 v112, v112, v1
	buffer_load_dwordx4 v[48:51], v112, s[36:39], 0 offen
	v_pk_mul_f32 v[152:153], v[148:149], v[116:117] op_sel_hi:[0,1]
	v_pk_mul_f32 v[154:155], v[148:149], v[118:119] op_sel_hi:[0,1]
	v_pk_mul_f32 v[156:157], v[148:149], v[120:121] op_sel_hi:[0,1]
	v_pk_mul_f32 v[158:159], v[148:149], v[122:123] op_sel_hi:[0,1]
	v_pk_mul_f32 v[160:161], v[148:149], v[124:125] op_sel_hi:[0,1]
	v_pk_mul_f32 v[162:163], v[148:149], v[126:127] op_sel_hi:[0,1]
	v_pk_mul_f32 v[164:165], v[148:149], v[128:129] op_sel_hi:[0,1]
	v_pk_mul_f32 v[166:167], v[148:149], v[130:131] op_sel_hi:[0,1]
	s_waitcnt vmcnt(20)
	v_cvt_pk_f32_fp8_e32 v[132:133], v52
	v_cvt_pk_f32_fp8_sdwa v[134:135], v52 src0_sel:WORD_1
	v_cvt_pk_f32_fp8_e32 v[136:137], v53
	v_cvt_pk_f32_fp8_sdwa v[138:139], v53 src0_sel:WORD_1
	v_cvt_pk_f32_fp8_e32 v[140:141], v54
	v_cvt_pk_f32_fp8_sdwa v[142:143], v54 src0_sel:WORD_1
	v_cvt_pk_f32_fp8_e32 v[144:145], v55
	v_cvt_pk_f32_fp8_sdwa v[146:147], v55 src0_sel:WORD_1
	v_and_b32_e32 v150, 0xffff0000, v32
	v_lshlrev_b32_sdwa v113, s47, v8 dst_sel:DWORD dst_unused:UNUSED_PAD src0_sel:DWORD src1_sel:WORD_1
	v_or_b32_e32 v113, v113, v1
	buffer_load_dwordx4 v[52:55], v113, s[36:39], 0 offen
	v_pk_fma_f32 v[152:153], v[150:151], v[132:133], v[152:153] op_sel_hi:[0,1,1]
	v_pk_fma_f32 v[154:155], v[150:151], v[134:135], v[154:155] op_sel_hi:[0,1,1]
	v_pk_fma_f32 v[156:157], v[150:151], v[136:137], v[156:157] op_sel_hi:[0,1,1]
	v_pk_fma_f32 v[158:159], v[150:151], v[138:139], v[158:159] op_sel_hi:[0,1,1]
	v_pk_fma_f32 v[160:161], v[150:151], v[140:141], v[160:161] op_sel_hi:[0,1,1]
	v_pk_fma_f32 v[162:163], v[150:151], v[142:143], v[162:163] op_sel_hi:[0,1,1]
	v_pk_fma_f32 v[164:165], v[150:151], v[144:145], v[164:165] op_sel_hi:[0,1,1]
	v_pk_fma_f32 v[166:167], v[150:151], v[146:147], v[166:167] op_sel_hi:[0,1,1]
	s_waitcnt vmcnt(20)
	v_cvt_pk_f32_fp8_e32 v[116:117], v56
	v_cvt_pk_f32_fp8_sdwa v[118:119], v56 src0_sel:WORD_1
	v_cvt_pk_f32_fp8_e32 v[120:121], v57
	v_cvt_pk_f32_fp8_sdwa v[122:123], v57 src0_sel:WORD_1
	v_cvt_pk_f32_fp8_e32 v[124:125], v58
	v_cvt_pk_f32_fp8_sdwa v[126:127], v58 src0_sel:WORD_1
	v_cvt_pk_f32_fp8_e32 v[128:129], v59
	v_cvt_pk_f32_fp8_sdwa v[130:131], v59 src0_sel:WORD_1
	v_lshlrev_b32_e32 v148, 16, v33
	v_lshlrev_b32_sdwa v112, s47, v9 dst_sel:DWORD dst_unused:UNUSED_PAD src0_sel:DWORD src1_sel:WORD_0
	v_or_b32_e32 v112, v112, v1
	buffer_load_dwordx4 v[56:59], v112, s[36:39], 0 offen
	v_pk_fma_f32 v[152:153], v[148:149], v[116:117], v[152:153] op_sel_hi:[0,1,1]
	v_pk_fma_f32 v[154:155], v[148:149], v[118:119], v[154:155] op_sel_hi:[0,1,1]
	v_pk_fma_f32 v[156:157], v[148:149], v[120:121], v[156:157] op_sel_hi:[0,1,1]
	v_pk_fma_f32 v[158:159], v[148:149], v[122:123], v[158:159] op_sel_hi:[0,1,1]
	v_pk_fma_f32 v[160:161], v[148:149], v[124:125], v[160:161] op_sel_hi:[0,1,1]
	v_pk_fma_f32 v[162:163], v[148:149], v[126:127], v[162:163] op_sel_hi:[0,1,1]
	v_pk_fma_f32 v[164:165], v[148:149], v[128:129], v[164:165] op_sel_hi:[0,1,1]
	v_pk_fma_f32 v[166:167], v[148:149], v[130:131], v[166:167] op_sel_hi:[0,1,1]
	s_waitcnt vmcnt(20)
	v_cvt_pk_f32_fp8_e32 v[132:133], v60
	v_cvt_pk_f32_fp8_sdwa v[134:135], v60 src0_sel:WORD_1
	v_cvt_pk_f32_fp8_e32 v[136:137], v61
	v_cvt_pk_f32_fp8_sdwa v[138:139], v61 src0_sel:WORD_1
	v_cvt_pk_f32_fp8_e32 v[140:141], v62
	v_cvt_pk_f32_fp8_sdwa v[142:143], v62 src0_sel:WORD_1
	v_cvt_pk_f32_fp8_e32 v[144:145], v63
	v_cvt_pk_f32_fp8_sdwa v[146:147], v63 src0_sel:WORD_1
	v_and_b32_e32 v150, 0xffff0000, v33
	v_lshlrev_b32_sdwa v113, s47, v9 dst_sel:DWORD dst_unused:UNUSED_PAD src0_sel:DWORD src1_sel:WORD_1
	v_or_b32_e32 v113, v113, v1
	buffer_load_dwordx4 v[60:63], v113, s[36:39], 0 offen
	v_pk_fma_f32 v[152:153], v[150:151], v[132:133], v[152:153] op_sel_hi:[0,1,1]
	v_pk_fma_f32 v[154:155], v[150:151], v[134:135], v[154:155] op_sel_hi:[0,1,1]
	v_pk_fma_f32 v[156:157], v[150:151], v[136:137], v[156:157] op_sel_hi:[0,1,1]
	v_pk_fma_f32 v[158:159], v[150:151], v[138:139], v[158:159] op_sel_hi:[0,1,1]
	v_pk_fma_f32 v[160:161], v[150:151], v[140:141], v[160:161] op_sel_hi:[0,1,1]
	v_pk_fma_f32 v[162:163], v[150:151], v[142:143], v[162:163] op_sel_hi:[0,1,1]
	v_pk_fma_f32 v[164:165], v[150:151], v[144:145], v[164:165] op_sel_hi:[0,1,1]
	v_pk_fma_f32 v[166:167], v[150:151], v[146:147], v[166:167] op_sel_hi:[0,1,1]
	s_waitcnt vmcnt(20)
	v_cvt_pk_f32_fp8_e32 v[116:117], v64
	v_cvt_pk_f32_fp8_sdwa v[118:119], v64 src0_sel:WORD_1
	v_cvt_pk_f32_fp8_e32 v[120:121], v65
	v_cvt_pk_f32_fp8_sdwa v[122:123], v65 src0_sel:WORD_1
	v_cvt_pk_f32_fp8_e32 v[124:125], v66
	v_cvt_pk_f32_fp8_sdwa v[126:127], v66 src0_sel:WORD_1
	v_cvt_pk_f32_fp8_e32 v[128:129], v67
	v_cvt_pk_f32_fp8_sdwa v[130:131], v67 src0_sel:WORD_1
	v_lshlrev_b32_e32 v148, 16, v34
	v_lshlrev_b32_sdwa v112, s47, v10 dst_sel:DWORD dst_unused:UNUSED_PAD src0_sel:DWORD src1_sel:WORD_0
	v_or_b32_e32 v112, v112, v1
	buffer_load_dwordx4 v[64:67], v112, s[36:39], 0 offen
	v_pk_fma_f32 v[152:153], v[148:149], v[116:117], v[152:153] op_sel_hi:[0,1,1]
	v_pk_fma_f32 v[154:155], v[148:149], v[118:119], v[154:155] op_sel_hi:[0,1,1]
	v_pk_fma_f32 v[156:157], v[148:149], v[120:121], v[156:157] op_sel_hi:[0,1,1]
	v_pk_fma_f32 v[158:159], v[148:149], v[122:123], v[158:159] op_sel_hi:[0,1,1]
	v_pk_fma_f32 v[160:161], v[148:149], v[124:125], v[160:161] op_sel_hi:[0,1,1]
	v_pk_fma_f32 v[162:163], v[148:149], v[126:127], v[162:163] op_sel_hi:[0,1,1]
	v_pk_fma_f32 v[164:165], v[148:149], v[128:129], v[164:165] op_sel_hi:[0,1,1]
	v_pk_fma_f32 v[166:167], v[148:149], v[130:131], v[166:167] op_sel_hi:[0,1,1]
	s_waitcnt vmcnt(20)
	v_cvt_pk_f32_fp8_e32 v[132:133], v68
	v_cvt_pk_f32_fp8_sdwa v[134:135], v68 src0_sel:WORD_1
	v_cvt_pk_f32_fp8_e32 v[136:137], v69
	v_cvt_pk_f32_fp8_sdwa v[138:139], v69 src0_sel:WORD_1
	v_cvt_pk_f32_fp8_e32 v[140:141], v70
	v_cvt_pk_f32_fp8_sdwa v[142:143], v70 src0_sel:WORD_1
	v_cvt_pk_f32_fp8_e32 v[144:145], v71
	v_cvt_pk_f32_fp8_sdwa v[146:147], v71 src0_sel:WORD_1
	v_and_b32_e32 v150, 0xffff0000, v34
	v_lshlrev_b32_sdwa v113, s47, v10 dst_sel:DWORD dst_unused:UNUSED_PAD src0_sel:DWORD src1_sel:WORD_1
	v_or_b32_e32 v113, v113, v1
	buffer_load_dwordx4 v[68:71], v113, s[36:39], 0 offen
	v_pk_fma_f32 v[152:153], v[150:151], v[132:133], v[152:153] op_sel_hi:[0,1,1]
	v_pk_fma_f32 v[154:155], v[150:151], v[134:135], v[154:155] op_sel_hi:[0,1,1]
	v_pk_fma_f32 v[156:157], v[150:151], v[136:137], v[156:157] op_sel_hi:[0,1,1]
	v_pk_fma_f32 v[158:159], v[150:151], v[138:139], v[158:159] op_sel_hi:[0,1,1]
	v_pk_fma_f32 v[160:161], v[150:151], v[140:141], v[160:161] op_sel_hi:[0,1,1]
	v_pk_fma_f32 v[162:163], v[150:151], v[142:143], v[162:163] op_sel_hi:[0,1,1]
	v_pk_fma_f32 v[164:165], v[150:151], v[144:145], v[164:165] op_sel_hi:[0,1,1]
	v_pk_fma_f32 v[166:167], v[150:151], v[146:147], v[166:167] op_sel_hi:[0,1,1]
	s_waitcnt vmcnt(20)
	v_cvt_pk_f32_fp8_e32 v[116:117], v72
	v_cvt_pk_f32_fp8_sdwa v[118:119], v72 src0_sel:WORD_1
	v_cvt_pk_f32_fp8_e32 v[120:121], v73
	v_cvt_pk_f32_fp8_sdwa v[122:123], v73 src0_sel:WORD_1
	v_cvt_pk_f32_fp8_e32 v[124:125], v74
	v_cvt_pk_f32_fp8_sdwa v[126:127], v74 src0_sel:WORD_1
	v_cvt_pk_f32_fp8_e32 v[128:129], v75
	v_cvt_pk_f32_fp8_sdwa v[130:131], v75 src0_sel:WORD_1
	v_lshlrev_b32_e32 v148, 16, v35
	v_lshlrev_b32_sdwa v112, s47, v11 dst_sel:DWORD dst_unused:UNUSED_PAD src0_sel:DWORD src1_sel:WORD_0
	v_or_b32_e32 v112, v112, v1
	buffer_load_dwordx4 v[72:75], v112, s[36:39], 0 offen
	v_pk_fma_f32 v[152:153], v[148:149], v[116:117], v[152:153] op_sel_hi:[0,1,1]
	v_pk_fma_f32 v[154:155], v[148:149], v[118:119], v[154:155] op_sel_hi:[0,1,1]
	v_pk_fma_f32 v[156:157], v[148:149], v[120:121], v[156:157] op_sel_hi:[0,1,1]
	v_pk_fma_f32 v[158:159], v[148:149], v[122:123], v[158:159] op_sel_hi:[0,1,1]
	v_pk_fma_f32 v[160:161], v[148:149], v[124:125], v[160:161] op_sel_hi:[0,1,1]
	v_pk_fma_f32 v[162:163], v[148:149], v[126:127], v[162:163] op_sel_hi:[0,1,1]
	v_pk_fma_f32 v[164:165], v[148:149], v[128:129], v[164:165] op_sel_hi:[0,1,1]
	v_pk_fma_f32 v[166:167], v[148:149], v[130:131], v[166:167] op_sel_hi:[0,1,1]
	s_waitcnt vmcnt(20)
	v_cvt_pk_f32_fp8_e32 v[132:133], v76
	v_cvt_pk_f32_fp8_sdwa v[134:135], v76 src0_sel:WORD_1
	v_cvt_pk_f32_fp8_e32 v[136:137], v77
	v_cvt_pk_f32_fp8_sdwa v[138:139], v77 src0_sel:WORD_1
	v_cvt_pk_f32_fp8_e32 v[140:141], v78
	v_cvt_pk_f32_fp8_sdwa v[142:143], v78 src0_sel:WORD_1
	v_cvt_pk_f32_fp8_e32 v[144:145], v79
	v_cvt_pk_f32_fp8_sdwa v[146:147], v79 src0_sel:WORD_1
	v_and_b32_e32 v150, 0xffff0000, v35
	v_lshlrev_b32_sdwa v113, s47, v11 dst_sel:DWORD dst_unused:UNUSED_PAD src0_sel:DWORD src1_sel:WORD_1
	v_or_b32_e32 v113, v113, v1
	buffer_load_dwordx4 v[76:79], v113, s[36:39], 0 offen
	v_pk_fma_f32 v[152:153], v[150:151], v[132:133], v[152:153] op_sel_hi:[0,1,1]
	v_pk_fma_f32 v[154:155], v[150:151], v[134:135], v[154:155] op_sel_hi:[0,1,1]
	v_pk_fma_f32 v[156:157], v[150:151], v[136:137], v[156:157] op_sel_hi:[0,1,1]
	v_pk_fma_f32 v[158:159], v[150:151], v[138:139], v[158:159] op_sel_hi:[0,1,1]
	v_pk_fma_f32 v[160:161], v[150:151], v[140:141], v[160:161] op_sel_hi:[0,1,1]
	v_pk_fma_f32 v[162:163], v[150:151], v[142:143], v[162:163] op_sel_hi:[0,1,1]
	v_pk_fma_f32 v[164:165], v[150:151], v[144:145], v[164:165] op_sel_hi:[0,1,1]
	v_pk_fma_f32 v[166:167], v[150:151], v[146:147], v[166:167] op_sel_hi:[0,1,1]
	s_waitcnt vmcnt(20)
	v_cvt_pk_f32_fp8_e32 v[116:117], v80
	v_cvt_pk_f32_fp8_sdwa v[118:119], v80 src0_sel:WORD_1
	v_cvt_pk_f32_fp8_e32 v[120:121], v81
	v_cvt_pk_f32_fp8_sdwa v[122:123], v81 src0_sel:WORD_1
	v_cvt_pk_f32_fp8_e32 v[124:125], v82
	v_cvt_pk_f32_fp8_sdwa v[126:127], v82 src0_sel:WORD_1
	v_cvt_pk_f32_fp8_e32 v[128:129], v83
	v_cvt_pk_f32_fp8_sdwa v[130:131], v83 src0_sel:WORD_1
	v_lshlrev_b32_e32 v148, 16, v36
	v_lshlrev_b32_sdwa v112, s47, v12 dst_sel:DWORD dst_unused:UNUSED_PAD src0_sel:DWORD src1_sel:WORD_0
	v_or_b32_e32 v112, v112, v1
	buffer_load_dwordx4 v[80:83], v112, s[36:39], 0 offen
	v_pk_fma_f32 v[152:153], v[148:149], v[116:117], v[152:153] op_sel_hi:[0,1,1]
	v_pk_fma_f32 v[154:155], v[148:149], v[118:119], v[154:155] op_sel_hi:[0,1,1]
	v_pk_fma_f32 v[156:157], v[148:149], v[120:121], v[156:157] op_sel_hi:[0,1,1]
	v_pk_fma_f32 v[158:159], v[148:149], v[122:123], v[158:159] op_sel_hi:[0,1,1]
	v_pk_fma_f32 v[160:161], v[148:149], v[124:125], v[160:161] op_sel_hi:[0,1,1]
	v_pk_fma_f32 v[162:163], v[148:149], v[126:127], v[162:163] op_sel_hi:[0,1,1]
	v_pk_fma_f32 v[164:165], v[148:149], v[128:129], v[164:165] op_sel_hi:[0,1,1]
	v_pk_fma_f32 v[166:167], v[148:149], v[130:131], v[166:167] op_sel_hi:[0,1,1]
	s_waitcnt vmcnt(20)
	v_cvt_pk_f32_fp8_e32 v[132:133], v84
	v_cvt_pk_f32_fp8_sdwa v[134:135], v84 src0_sel:WORD_1
	v_cvt_pk_f32_fp8_e32 v[136:137], v85
	v_cvt_pk_f32_fp8_sdwa v[138:139], v85 src0_sel:WORD_1
	v_cvt_pk_f32_fp8_e32 v[140:141], v86
	v_cvt_pk_f32_fp8_sdwa v[142:143], v86 src0_sel:WORD_1
	v_cvt_pk_f32_fp8_e32 v[144:145], v87
	v_cvt_pk_f32_fp8_sdwa v[146:147], v87 src0_sel:WORD_1
	v_and_b32_e32 v150, 0xffff0000, v36
	v_lshlrev_b32_sdwa v113, s47, v12 dst_sel:DWORD dst_unused:UNUSED_PAD src0_sel:DWORD src1_sel:WORD_1
	v_or_b32_e32 v113, v113, v1
	buffer_load_dwordx4 v[84:87], v113, s[36:39], 0 offen
	v_pk_fma_f32 v[152:153], v[150:151], v[132:133], v[152:153] op_sel_hi:[0,1,1]
	v_pk_fma_f32 v[154:155], v[150:151], v[134:135], v[154:155] op_sel_hi:[0,1,1]
	v_pk_fma_f32 v[156:157], v[150:151], v[136:137], v[156:157] op_sel_hi:[0,1,1]
	v_pk_fma_f32 v[158:159], v[150:151], v[138:139], v[158:159] op_sel_hi:[0,1,1]
	v_pk_fma_f32 v[160:161], v[150:151], v[140:141], v[160:161] op_sel_hi:[0,1,1]
	v_pk_fma_f32 v[162:163], v[150:151], v[142:143], v[162:163] op_sel_hi:[0,1,1]
	v_pk_fma_f32 v[164:165], v[150:151], v[144:145], v[164:165] op_sel_hi:[0,1,1]
	v_pk_fma_f32 v[166:167], v[150:151], v[146:147], v[166:167] op_sel_hi:[0,1,1]
	s_waitcnt vmcnt(20)
	v_cvt_pk_f32_fp8_e32 v[116:117], v88
	v_cvt_pk_f32_fp8_sdwa v[118:119], v88 src0_sel:WORD_1
	v_cvt_pk_f32_fp8_e32 v[120:121], v89
	v_cvt_pk_f32_fp8_sdwa v[122:123], v89 src0_sel:WORD_1
	v_cvt_pk_f32_fp8_e32 v[124:125], v90
	v_cvt_pk_f32_fp8_sdwa v[126:127], v90 src0_sel:WORD_1
	v_cvt_pk_f32_fp8_e32 v[128:129], v91
	v_cvt_pk_f32_fp8_sdwa v[130:131], v91 src0_sel:WORD_1
	v_lshlrev_b32_e32 v148, 16, v37
	v_lshlrev_b32_sdwa v112, s47, v13 dst_sel:DWORD dst_unused:UNUSED_PAD src0_sel:DWORD src1_sel:WORD_0
	v_or_b32_e32 v112, v112, v1
	buffer_load_dwordx4 v[88:91], v112, s[36:39], 0 offen
	v_pk_fma_f32 v[152:153], v[148:149], v[116:117], v[152:153] op_sel_hi:[0,1,1]
	v_pk_fma_f32 v[154:155], v[148:149], v[118:119], v[154:155] op_sel_hi:[0,1,1]
	v_pk_fma_f32 v[156:157], v[148:149], v[120:121], v[156:157] op_sel_hi:[0,1,1]
	v_pk_fma_f32 v[158:159], v[148:149], v[122:123], v[158:159] op_sel_hi:[0,1,1]
	v_pk_fma_f32 v[160:161], v[148:149], v[124:125], v[160:161] op_sel_hi:[0,1,1]
	v_pk_fma_f32 v[162:163], v[148:149], v[126:127], v[162:163] op_sel_hi:[0,1,1]
	v_pk_fma_f32 v[164:165], v[148:149], v[128:129], v[164:165] op_sel_hi:[0,1,1]
	v_pk_fma_f32 v[166:167], v[148:149], v[130:131], v[166:167] op_sel_hi:[0,1,1]
	s_waitcnt vmcnt(20)
	v_cvt_pk_f32_fp8_e32 v[132:133], v92
	v_cvt_pk_f32_fp8_sdwa v[134:135], v92 src0_sel:WORD_1
	v_cvt_pk_f32_fp8_e32 v[136:137], v93
	v_cvt_pk_f32_fp8_sdwa v[138:139], v93 src0_sel:WORD_1
	v_cvt_pk_f32_fp8_e32 v[140:141], v94
	v_cvt_pk_f32_fp8_sdwa v[142:143], v94 src0_sel:WORD_1
	v_cvt_pk_f32_fp8_e32 v[144:145], v95
	v_cvt_pk_f32_fp8_sdwa v[146:147], v95 src0_sel:WORD_1
	v_and_b32_e32 v150, 0xffff0000, v37
	v_lshlrev_b32_sdwa v113, s47, v13 dst_sel:DWORD dst_unused:UNUSED_PAD src0_sel:DWORD src1_sel:WORD_1
	v_or_b32_e32 v113, v113, v1
	buffer_load_dwordx4 v[92:95], v113, s[36:39], 0 offen
	v_pk_fma_f32 v[152:153], v[150:151], v[132:133], v[152:153] op_sel_hi:[0,1,1]
	v_pk_fma_f32 v[154:155], v[150:151], v[134:135], v[154:155] op_sel_hi:[0,1,1]
	v_pk_fma_f32 v[156:157], v[150:151], v[136:137], v[156:157] op_sel_hi:[0,1,1]
	v_pk_fma_f32 v[158:159], v[150:151], v[138:139], v[158:159] op_sel_hi:[0,1,1]
	v_pk_fma_f32 v[160:161], v[150:151], v[140:141], v[160:161] op_sel_hi:[0,1,1]
	v_pk_fma_f32 v[162:163], v[150:151], v[142:143], v[162:163] op_sel_hi:[0,1,1]
	v_pk_fma_f32 v[164:165], v[150:151], v[144:145], v[164:165] op_sel_hi:[0,1,1]
	v_pk_fma_f32 v[166:167], v[150:151], v[146:147], v[166:167] op_sel_hi:[0,1,1]
	s_waitcnt vmcnt(20)
	v_cvt_pk_f32_fp8_e32 v[116:117], v96
	v_cvt_pk_f32_fp8_sdwa v[118:119], v96 src0_sel:WORD_1
	v_cvt_pk_f32_fp8_e32 v[120:121], v97
	v_cvt_pk_f32_fp8_sdwa v[122:123], v97 src0_sel:WORD_1
	v_cvt_pk_f32_fp8_e32 v[124:125], v98
	v_cvt_pk_f32_fp8_sdwa v[126:127], v98 src0_sel:WORD_1
	v_cvt_pk_f32_fp8_e32 v[128:129], v99
	v_cvt_pk_f32_fp8_sdwa v[130:131], v99 src0_sel:WORD_1
	v_lshlrev_b32_e32 v148, 16, v38
	v_lshlrev_b32_sdwa v112, s47, v14 dst_sel:DWORD dst_unused:UNUSED_PAD src0_sel:DWORD src1_sel:WORD_0
	v_or_b32_e32 v112, v112, v1
	buffer_load_dwordx4 v[96:99], v112, s[36:39], 0 offen
	v_pk_fma_f32 v[152:153], v[148:149], v[116:117], v[152:153] op_sel_hi:[0,1,1]
	v_pk_fma_f32 v[154:155], v[148:149], v[118:119], v[154:155] op_sel_hi:[0,1,1]
	v_pk_fma_f32 v[156:157], v[148:149], v[120:121], v[156:157] op_sel_hi:[0,1,1]
	v_pk_fma_f32 v[158:159], v[148:149], v[122:123], v[158:159] op_sel_hi:[0,1,1]
	v_pk_fma_f32 v[160:161], v[148:149], v[124:125], v[160:161] op_sel_hi:[0,1,1]
	v_pk_fma_f32 v[162:163], v[148:149], v[126:127], v[162:163] op_sel_hi:[0,1,1]
	v_pk_fma_f32 v[164:165], v[148:149], v[128:129], v[164:165] op_sel_hi:[0,1,1]
	v_pk_fma_f32 v[166:167], v[148:149], v[130:131], v[166:167] op_sel_hi:[0,1,1]
	s_waitcnt vmcnt(20)
	v_cvt_pk_f32_fp8_e32 v[132:133], v100
	v_cvt_pk_f32_fp8_sdwa v[134:135], v100 src0_sel:WORD_1
	v_cvt_pk_f32_fp8_e32 v[136:137], v101
	v_cvt_pk_f32_fp8_sdwa v[138:139], v101 src0_sel:WORD_1
	v_cvt_pk_f32_fp8_e32 v[140:141], v102
	v_cvt_pk_f32_fp8_sdwa v[142:143], v102 src0_sel:WORD_1
	v_cvt_pk_f32_fp8_e32 v[144:145], v103
	v_cvt_pk_f32_fp8_sdwa v[146:147], v103 src0_sel:WORD_1
	v_and_b32_e32 v150, 0xffff0000, v38
	v_lshlrev_b32_sdwa v113, s47, v14 dst_sel:DWORD dst_unused:UNUSED_PAD src0_sel:DWORD src1_sel:WORD_1
	v_or_b32_e32 v113, v113, v1
	buffer_load_dwordx4 v[100:103], v113, s[36:39], 0 offen
	v_pk_fma_f32 v[152:153], v[150:151], v[132:133], v[152:153] op_sel_hi:[0,1,1]
	v_pk_fma_f32 v[154:155], v[150:151], v[134:135], v[154:155] op_sel_hi:[0,1,1]
	v_pk_fma_f32 v[156:157], v[150:151], v[136:137], v[156:157] op_sel_hi:[0,1,1]
	v_pk_fma_f32 v[158:159], v[150:151], v[138:139], v[158:159] op_sel_hi:[0,1,1]
	v_pk_fma_f32 v[160:161], v[150:151], v[140:141], v[160:161] op_sel_hi:[0,1,1]
	v_pk_fma_f32 v[162:163], v[150:151], v[142:143], v[162:163] op_sel_hi:[0,1,1]
	v_pk_fma_f32 v[164:165], v[150:151], v[144:145], v[164:165] op_sel_hi:[0,1,1]
	v_pk_fma_f32 v[166:167], v[150:151], v[146:147], v[166:167] op_sel_hi:[0,1,1]
	s_waitcnt vmcnt(20)
	v_cvt_pk_f32_fp8_e32 v[116:117], v104
	v_cvt_pk_f32_fp8_sdwa v[118:119], v104 src0_sel:WORD_1
	v_cvt_pk_f32_fp8_e32 v[120:121], v105
	v_cvt_pk_f32_fp8_sdwa v[122:123], v105 src0_sel:WORD_1
	v_cvt_pk_f32_fp8_e32 v[124:125], v106
	v_cvt_pk_f32_fp8_sdwa v[126:127], v106 src0_sel:WORD_1
	v_cvt_pk_f32_fp8_e32 v[128:129], v107
	v_cvt_pk_f32_fp8_sdwa v[130:131], v107 src0_sel:WORD_1
	v_lshlrev_b32_e32 v148, 16, v39
	v_lshlrev_b32_sdwa v112, s47, v15 dst_sel:DWORD dst_unused:UNUSED_PAD src0_sel:DWORD src1_sel:WORD_0
	v_or_b32_e32 v112, v112, v1
	buffer_load_dwordx4 v[104:107], v112, s[36:39], 0 offen
	v_pk_fma_f32 v[152:153], v[148:149], v[116:117], v[152:153] op_sel_hi:[0,1,1]
	v_pk_fma_f32 v[154:155], v[148:149], v[118:119], v[154:155] op_sel_hi:[0,1,1]
	v_pk_fma_f32 v[156:157], v[148:149], v[120:121], v[156:157] op_sel_hi:[0,1,1]
	v_pk_fma_f32 v[158:159], v[148:149], v[122:123], v[158:159] op_sel_hi:[0,1,1]
	v_pk_fma_f32 v[160:161], v[148:149], v[124:125], v[160:161] op_sel_hi:[0,1,1]
	v_pk_fma_f32 v[162:163], v[148:149], v[126:127], v[162:163] op_sel_hi:[0,1,1]
	v_pk_fma_f32 v[164:165], v[148:149], v[128:129], v[164:165] op_sel_hi:[0,1,1]
	v_pk_fma_f32 v[166:167], v[148:149], v[130:131], v[166:167] op_sel_hi:[0,1,1]
	s_waitcnt vmcnt(20)
	v_cvt_pk_f32_fp8_e32 v[132:133], v108
	v_cvt_pk_f32_fp8_sdwa v[134:135], v108 src0_sel:WORD_1
	v_cvt_pk_f32_fp8_e32 v[136:137], v109
	v_cvt_pk_f32_fp8_sdwa v[138:139], v109 src0_sel:WORD_1
	v_cvt_pk_f32_fp8_e32 v[140:141], v110
	v_cvt_pk_f32_fp8_sdwa v[142:143], v110 src0_sel:WORD_1
	v_cvt_pk_f32_fp8_e32 v[144:145], v111
	v_cvt_pk_f32_fp8_sdwa v[146:147], v111 src0_sel:WORD_1
	v_and_b32_e32 v150, 0xffff0000, v39
	v_lshlrev_b32_sdwa v113, s47, v15 dst_sel:DWORD dst_unused:UNUSED_PAD src0_sel:DWORD src1_sel:WORD_1
	v_or_b32_e32 v113, v113, v1
	buffer_load_dwordx4 v[108:111], v113, s[36:39], 0 offen
	v_pk_fma_f32 v[152:153], v[150:151], v[132:133], v[152:153] op_sel_hi:[0,1,1]
	v_pk_fma_f32 v[154:155], v[150:151], v[134:135], v[154:155] op_sel_hi:[0,1,1]
	v_pk_fma_f32 v[156:157], v[150:151], v[136:137], v[156:157] op_sel_hi:[0,1,1]
	v_pk_fma_f32 v[158:159], v[150:151], v[138:139], v[158:159] op_sel_hi:[0,1,1]
	v_pk_fma_f32 v[160:161], v[150:151], v[140:141], v[160:161] op_sel_hi:[0,1,1]
	v_pk_fma_f32 v[162:163], v[150:151], v[142:143], v[162:163] op_sel_hi:[0,1,1]
	v_pk_fma_f32 v[164:165], v[150:151], v[144:145], v[164:165] op_sel_hi:[0,1,1]
	v_pk_fma_f32 v[166:167], v[150:151], v[146:147], v[166:167] op_sel_hi:[0,1,1]
	s_nop 1
	v_permlane32_swap_b32_e32 v152, v160
	v_permlane32_swap_b32_e32 v153, v161
	v_permlane32_swap_b32_e32 v154, v162
	v_permlane32_swap_b32_e32 v155, v163
	v_permlane32_swap_b32_e32 v156, v164
	v_permlane32_swap_b32_e32 v157, v165
	v_permlane32_swap_b32_e32 v158, v166
	v_permlane32_swap_b32_e32 v159, v167
	v_add_f32_e32 v168, v152, v160
	v_add_f32_e32 v169, v153, v161
	v_add_f32_e32 v170, v154, v162
	v_add_f32_e32 v171, v155, v163
	v_add_f32_e32 v172, v156, v164
	v_add_f32_e32 v173, v157, v165
	v_add_f32_e32 v174, v158, v166
	v_add_f32_e32 v175, v159, v167
	s_nop 1
	v_permlane16_swap_b32_e32 v168, v172
	v_permlane16_swap_b32_e32 v169, v173
	v_permlane16_swap_b32_e32 v170, v174
	v_permlane16_swap_b32_e32 v171, v175
	v_add_f32_e32 v176, v168, v172
	v_add_f32_e32 v177, v169, v173
	v_add_f32_e32 v178, v170, v174
	v_add_f32_e32 v179, v171, v175
	v_cndmask_b32_e64 v180, v176, v178, s[44:45]
	v_cndmask_b32_e64 v181, v177, v179, s[44:45]
	v_cndmask_b32_e64 v182, v178, v176, s[44:45]
	v_cndmask_b32_e64 v183, v179, v177, s[44:45]
	s_nop 0
	v_add_f32_dpp v184, v180, v182 row_ror:8 row_mask:0xf bank_mask:0xf
	v_add_f32_dpp v185, v181, v183 row_ror:8 row_mask:0xf bank_mask:0xf
	v_cvt_pk_bf16_f32 v186, v184, v185
	s_lshl_b32 s2, s20, 12
	s_add_u32 s2, s34, s2
	s_addc_u32 s3, s35, 0
	global_store_dword v3, v186, s[2:3]
	s_mov_b32 s20, s21
	s_mov_b32 s48, s49
	s_mov_b32 s21, s22
	s_mov_b32 s49, s50
	s_cmp_eq_u32 s48, 0
	s_cbranch_scc1 .Lv_drain
	s_branch .Lv_loop
.Lv_drain:
.Lv_next_slice:
	s_waitcnt vmcnt(0)
	s_add_u32 s17, s17, 1
	s_add_u32 s16, s16, 1
	s_cmp_lt_u32 s17, 2
	s_cbranch_scc1 .Lv_slice
.LBB0_1215:
	s_cmp_gt_i32 s41, 13
	s_cselect_b64 s[2:3], -1, 0
	s_and_b64 s[4:5], s[14:15], s[2:3]
	s_andn2_b64 vcc, exec, s[4:5]
	s_cbranch_vccnz .LBB0_1269
	s_mov_b64 s[6:7], s[0:1]
	s_waitcnt vmcnt(0) lgkmcnt(0)
	v_mbcnt_lo_u32_b32 v0, -1, 0
	v_mbcnt_hi_u32_b32 v0, -1, v0
	s_waitcnt vmcnt(0)
	s_add_u32 s10, s0, 0xc8
	v_or_b32_e32 v0, s25, v0
	s_addc_u32 s11, s1, 0
	v_cmp_eq_u32_e32 vcc, 0, v0
	s_barrier
	s_and_saveexec_b64 s[4:5], vcc
	s_cbranch_execz .LBB0_1268
	s_mov_b64 s[8:9], src_shared_base
	s_load_dwordx2 s[6:7], s[6:7], 0xb8
	s_waitcnt vmcnt(0) expcnt(0) lgkmcnt(0)
	s_getreg_b32 s8, hwreg(HW_REG_XCC_ID, 0, 4)
	s_and_b32 s26, s8, 15
	s_add_i32 s27, 0, 0x23fc0
	s_cmp_lg_u32 s27, -1
	s_cselect_b32 s8, s27, 0
	s_cselect_b32 s12, s9, 0
	s_add_i32 s28, 0, 0x23fc4
	s_cmp_lg_u32 s28, -1
	v_mov_b32_e32 v0, s8
	v_mov_b32_e32 v1, s12
	s_cselect_b32 s8, s28, 0
	s_cselect_b32 s9, s9, 0
	flat_load_dword v2, v[0:1] sc0 sc1
	s_waitcnt vmcnt(0)
	v_mov_b32_e32 v0, s8
	v_mov_b32_e32 v1, s9
	flat_load_dword v0, v[0:1] sc0 sc1
	s_waitcnt vmcnt(0) lgkmcnt(0)
	v_cmp_eq_u32_e32 vcc, 0, v2
	s_and_saveexec_b64 s[8:9], vcc
	s_cbranch_execz .LBB0_1232
	s_load_dword s29, s[10:11], 0x0
	s_add_u32 s10, s6, 0x1000
	s_addc_u32 s11, s7, 0
	s_add_u32 s12, s6, 0x1100
	s_addc_u32 s13, s7, 0
	s_add_u32 s14, s6, 0x1200
	s_addc_u32 s15, s7, 0
	s_add_u32 s16, s6, 0x1300
	s_addc_u32 s17, s7, 0
	s_mov_b32 s30, 1
	v_mov_b32_e32 v16, 0
	s_branch .LBB0_1220
